# ROUTE router K-loop: removed the compiler's vmcnt(0) before the barrier; the source's counted vmcnt(4) now really leaves the next chunk's LDS-DMA loads in flight
# speedup vs baseline: 1.0134x; 1.0047x over previous
.LBB0_617:
	s_cmp_lt_u32 s49, 30
	s_mov_b64 s[46:47], -1
	s_waitcnt lgkmcnt(0)
	s_barrier
	s_cbranch_scc1 .LBB0_619
	s_lshl_b32 s50, s48, 15
	s_mov_b64 s[46:47], 0
